# all PEER table conversion deferred into the layer-0 GEMM windows, throttle sleeps removed
# speedup vs baseline: 1.0162x; 1.0162x over previous
.Ldfa_loop:
	s_add_u32 s11, s4, s10
	s_min_u32 s11, s11, 0x6bff
	s_mov_b32 s101, s11
	s_lshl_b32 s11, s101, 13
	v_add_u32_e32 v40, s11, v7
	v_add_u32_e32 v41, 0x1000, v40
	global_load_dwordx4 v[76:79], v40, s[8:9] nt
	global_load_dwordx4 v[80:83], v40, s[8:9] offset:1024 nt
	global_load_dwordx4 v[84:87], v40, s[8:9] offset:2048 nt
	global_load_dwordx4 v[88:91], v40, s[8:9] offset:3072 nt
	global_load_dwordx4 v[92:95], v41, s[8:9] nt
	global_load_dwordx4 v[96:99], v41, s[8:9] offset:1024 nt
	global_load_dwordx4 v[100:103], v41, s[8:9] offset:2048 nt
	global_load_dwordx4 v[104:107], v41, s[8:9] offset:3072 nt
	s_waitcnt vmcnt(8)
	v_max3_f32 v42, |v8|, |v9|, |v10|
	v_max3_f32 v43, |v12|, |v13|, |v14|
	v_max3_f32 v44, |v16|, |v17|, |v18|
	v_max3_f32 v45, |v20|, |v21|, |v22|
	v_max3_f32 v46, |v24|, |v25|, |v26|
	v_max3_f32 v47, |v28|, |v29|, |v30|
	v_max3_f32 v48, |v32|, |v33|, |v34|
	v_max3_f32 v49, |v36|, |v37|, |v38|
	v_max_f32_e64 v42, v42, |v11|
	v_max_f32_e64 v43, v43, |v15|
	v_max_f32_e64 v44, v44, |v19|
	v_max_f32_e64 v45, v45, |v23|
	v_max_f32_e64 v46, v46, |v27|
	v_max_f32_e64 v47, v47, |v31|
	v_max_f32_e64 v48, v48, |v35|
	v_max_f32_e64 v49, v49, |v39|
	v_max3_f32 v42, v42, v43, v44
	v_max3_f32 v45, v45, v46, v47
	v_max3_f32 v42, v42, v45, v48
	v_max_f32_e32 v42, v42, v49
	s_nop 1
	v_max_f32_dpp v43, v42, v42 quad_perm:[1,0,3,2] row_mask:0xf bank_mask:0xf bound_ctrl:1
	s_nop 1
	v_max_f32_dpp v42, v43, v43 quad_perm:[2,3,0,1] row_mask:0xf bank_mask:0xf bound_ctrl:1
	s_nop 1
	v_max_f32_dpp v43, v42, v42 row_half_mirror row_mask:0xf bank_mask:0xf bound_ctrl:1
	s_nop 1
	v_max_f32_dpp v42, v43, v43 row_mirror row_mask:0xf bank_mask:0xf bound_ctrl:1
	s_nop 1
	v_mov_b32_e32 v43, v42
	s_nop 1
	v_permlane16_swap_b32_e32 v42, v43
	v_max_f32_e32 v42, v42, v43
	v_mov_b32_e32 v43, v42
	s_nop 1
	v_permlane32_swap_b32_e32 v42, v43
	v_max_f32_e32 v49, v42, v43
	v_mul_f32_e32 v44, 0x3b124925, v49
	s_lshl_b32 s11, s4, 2
	s_add_u32 s11, s11, 0x12a00000
	v_mov_b32_e32 v45, s11
	s_mov_b64 exec, 1
	global_store_dword v45, v44, s[6:7]
	s_mov_b64 exec, -1
	v_mov_b32_e32 v46, 0x43e00000
	v_div_scale_f32 v42, s[100:101], v49, v49, v46
	v_rcp_f32_e32 v43, v42
	s_nop 0
	v_fma_f32 v44, -v42, v43, 1.0
	v_fmac_f32_e32 v43, v44, v43
	v_div_scale_f32 v44, vcc, v46, v49, v46
	v_mul_f32_e32 v45, v44, v43
	v_fma_f32 v47, -v42, v45, v44
	v_fmac_f32_e32 v45, v47, v43
	v_fma_f32 v42, -v42, v45, v44
	s_nop 1
	v_div_fmas_f32 v42, v42, v43, v45
	v_div_fixup_f32 v42, v42, v49, v46
	v_cmp_lt_f32_e32 vcc, 0, v49
	s_nop 1
	v_cndmask_b32_e32 v48, 0, v42, vcc
	v_mul_f32_e32 v8, v8, v48
	v_mul_f32_e32 v9, v9, v48
	v_mul_f32_e32 v10, v10, v48
	v_mul_f32_e32 v11, v11, v48
	v_mul_f32_e32 v12, v12, v48
	v_mul_f32_e32 v13, v13, v48
	v_mul_f32_e32 v14, v14, v48
	v_mul_f32_e32 v15, v15, v48
	v_mul_f32_e32 v16, v16, v48
	v_mul_f32_e32 v17, v17, v48
	v_mul_f32_e32 v18, v18, v48
	v_mul_f32_e32 v19, v19, v48
	v_mul_f32_e32 v20, v20, v48
	v_mul_f32_e32 v21, v21, v48
	v_mul_f32_e32 v22, v22, v48
	v_mul_f32_e32 v23, v23, v48
	v_mul_f32_e32 v24, v24, v48
	v_mul_f32_e32 v25, v25, v48
	v_mul_f32_e32 v26, v26, v48
	v_mul_f32_e32 v27, v27, v48
	v_mul_f32_e32 v28, v28, v48
	v_mul_f32_e32 v29, v29, v48
	v_mul_f32_e32 v30, v30, v48
	v_mul_f32_e32 v31, v31, v48
	v_mul_f32_e32 v32, v32, v48
	v_mul_f32_e32 v33, v33, v48
	v_mul_f32_e32 v34, v34, v48
	v_mul_f32_e32 v35, v35, v48
	v_mul_f32_e32 v36, v36, v48
	v_mul_f32_e32 v37, v37, v48
	v_mul_f32_e32 v38, v38, v48
	v_mul_f32_e32 v39, v39, v48
	v_mov_b32_e32 v58, 0
	v_mov_b32_e32 v59, 0
	v_mov_b32_e32 v60, 0
	v_mov_b32_e32 v61, 0
	v_mov_b32_e32 v62, 0
	v_mov_b32_e32 v63, 0
	v_mov_b32_e32 v64, 0
	v_mov_b32_e32 v65, 0
	v_cvt_pk_fp8_f32 v58, v8, v9
	v_cvt_pk_fp8_f32 v59, v12, v13
	v_cvt_pk_fp8_f32 v60, v16, v17
	v_cvt_pk_fp8_f32 v61, v20, v21
	v_cvt_pk_fp8_f32 v62, v24, v25
	v_cvt_pk_fp8_f32 v63, v28, v29
	v_cvt_pk_fp8_f32 v64, v32, v33
	v_cvt_pk_fp8_f32 v65, v36, v37
	v_cvt_pk_fp8_f32 v58, v10, v11 op_sel:[0,0,1]
	v_cvt_pk_fp8_f32 v59, v14, v15 op_sel:[0,0,1]
	v_cvt_pk_fp8_f32 v60, v18, v19 op_sel:[0,0,1]
	v_cvt_pk_fp8_f32 v61, v22, v23 op_sel:[0,0,1]
	v_cvt_pk_fp8_f32 v62, v26, v27 op_sel:[0,0,1]
	v_cvt_pk_fp8_f32 v63, v30, v31 op_sel:[0,0,1]
	v_cvt_pk_fp8_f32 v64, v34, v35 op_sel:[0,0,1]
	v_cvt_pk_fp8_f32 v65, v38, v39 op_sel:[0,0,1]
	s_and_b32 s11, s4, 0x3fff
	s_lshl_b32 s11, s11, 7
	s_lshr_b32 s101, s4, 14
	s_lshl_b32 s101, s101, 25
	s_add_u32 s11, s11, s101
	v_add_u32_e32 v66, s11, v56
	v_add_u32_e32 v67, 0x400000, v66
	v_add_u32_e32 v68, 0x800000, v66
	v_add_u32_e32 v69, 0xc00000, v66
	v_add_u32_e32 v70, 0x1000000, v66
	v_add_u32_e32 v71, 0x1400000, v66
	v_add_u32_e32 v72, 0x1800000, v66
	v_add_u32_e32 v73, 0x1c00000, v66
	global_store_dword v66, v58, s[6:7] nt
	global_store_dword v67, v59, s[6:7] nt
	global_store_dword v68, v60, s[6:7] nt
	global_store_dword v69, v61, s[6:7] nt
	global_store_dword v70, v62, s[6:7] nt
	global_store_dword v71, v63, s[6:7] nt
	global_store_dword v72, v64, s[6:7] nt
	global_store_dword v73, v65, s[6:7] nt
	s_add_u32 s4, s4, s10
	s_cmp_ge_u32 s4, 0x6c00
	s_cbranch_scc1 .Ldfa_done
	s_add_u32 s11, s4, s10
	s_min_u32 s11, s11, 0x6bff
	s_mov_b32 s101, s11
	s_lshl_b32 s11, s101, 13
	v_add_u32_e32 v40, s11, v7
	v_add_u32_e32 v41, 0x1000, v40
	global_load_dwordx4 v[8:11], v40, s[8:9] nt
	global_load_dwordx4 v[12:15], v40, s[8:9] offset:1024 nt
	global_load_dwordx4 v[16:19], v40, s[8:9] offset:2048 nt
	global_load_dwordx4 v[20:23], v40, s[8:9] offset:3072 nt
	global_load_dwordx4 v[24:27], v41, s[8:9] nt
	global_load_dwordx4 v[28:31], v41, s[8:9] offset:1024 nt
	global_load_dwordx4 v[32:35], v41, s[8:9] offset:2048 nt
	global_load_dwordx4 v[36:39], v41, s[8:9] offset:3072 nt
	s_waitcnt vmcnt(8)
	v_max3_f32 v42, |v76|, |v77|, |v78|
	v_max3_f32 v43, |v80|, |v81|, |v82|
	v_max3_f32 v44, |v84|, |v85|, |v86|
	v_max3_f32 v45, |v88|, |v89|, |v90|
	v_max3_f32 v46, |v92|, |v93|, |v94|
	v_max3_f32 v47, |v96|, |v97|, |v98|
	v_max3_f32 v48, |v100|, |v101|, |v102|
	v_max3_f32 v49, |v104|, |v105|, |v106|
	v_max_f32_e64 v42, v42, |v79|
	v_max_f32_e64 v43, v43, |v83|
	v_max_f32_e64 v44, v44, |v87|
	v_max_f32_e64 v45, v45, |v91|
	v_max_f32_e64 v46, v46, |v95|
	v_max_f32_e64 v47, v47, |v99|
	v_max_f32_e64 v48, v48, |v103|
	v_max_f32_e64 v49, v49, |v107|
	v_max3_f32 v42, v42, v43, v44
	v_max3_f32 v45, v45, v46, v47
	v_max3_f32 v42, v42, v45, v48
	v_max_f32_e32 v42, v42, v49
	s_nop 1
	v_max_f32_dpp v43, v42, v42 quad_perm:[1,0,3,2] row_mask:0xf bank_mask:0xf bound_ctrl:1
	s_nop 1
	v_max_f32_dpp v42, v43, v43 quad_perm:[2,3,0,1] row_mask:0xf bank_mask:0xf bound_ctrl:1
	s_nop 1
	v_max_f32_dpp v43, v42, v42 row_half_mirror row_mask:0xf bank_mask:0xf bound_ctrl:1
	s_nop 1
	v_max_f32_dpp v42, v43, v43 row_mirror row_mask:0xf bank_mask:0xf bound_ctrl:1
	s_nop 1
	v_mov_b32_e32 v43, v42
	s_nop 1
	v_permlane16_swap_b32_e32 v42, v43
	v_max_f32_e32 v42, v42, v43
	v_mov_b32_e32 v43, v42
	s_nop 1
	v_permlane32_swap_b32_e32 v42, v43
	v_max_f32_e32 v49, v42, v43
	v_mul_f32_e32 v44, 0x3b124925, v49
	s_lshl_b32 s11, s4, 2
	s_add_u32 s11, s11, 0x12a00000
	v_mov_b32_e32 v45, s11
	s_mov_b64 exec, 1
	global_store_dword v45, v44, s[6:7]
	s_mov_b64 exec, -1
	v_mov_b32_e32 v46, 0x43e00000
	v_div_scale_f32 v42, s[100:101], v49, v49, v46
	v_rcp_f32_e32 v43, v42
	s_nop 0
	v_fma_f32 v44, -v42, v43, 1.0
	v_fmac_f32_e32 v43, v44, v43
	v_div_scale_f32 v44, vcc, v46, v49, v46
	v_mul_f32_e32 v45, v44, v43
	v_fma_f32 v47, -v42, v45, v44
	v_fmac_f32_e32 v45, v47, v43
	v_fma_f32 v42, -v42, v45, v44
	s_nop 1
	v_div_fmas_f32 v42, v42, v43, v45
	v_div_fixup_f32 v42, v42, v49, v46
	v_cmp_lt_f32_e32 vcc, 0, v49
	s_nop 1
	v_cndmask_b32_e32 v48, 0, v42, vcc
	v_mul_f32_e32 v76, v76, v48
	v_mul_f32_e32 v77, v77, v48
	v_mul_f32_e32 v78, v78, v48
	v_mul_f32_e32 v79, v79, v48
	v_mul_f32_e32 v80, v80, v48
	v_mul_f32_e32 v81, v81, v48
	v_mul_f32_e32 v82, v82, v48
	v_mul_f32_e32 v83, v83, v48
	v_mul_f32_e32 v84, v84, v48
	v_mul_f32_e32 v85, v85, v48
	v_mul_f32_e32 v86, v86, v48
	v_mul_f32_e32 v87, v87, v48
	v_mul_f32_e32 v88, v88, v48
	v_mul_f32_e32 v89, v89, v48
	v_mul_f32_e32 v90, v90, v48
	v_mul_f32_e32 v91, v91, v48
	v_mul_f32_e32 v92, v92, v48
	v_mul_f32_e32 v93, v93, v48
	v_mul_f32_e32 v94, v94, v48
	v_mul_f32_e32 v95, v95, v48
	v_mul_f32_e32 v96, v96, v48
	v_mul_f32_e32 v97, v97, v48
	v_mul_f32_e32 v98, v98, v48
	v_mul_f32_e32 v99, v99, v48
	v_mul_f32_e32 v100, v100, v48
	v_mul_f32_e32 v101, v101, v48
	v_mul_f32_e32 v102, v102, v48
	v_mul_f32_e32 v103, v103, v48
	v_mul_f32_e32 v104, v104, v48
	v_mul_f32_e32 v105, v105, v48
	v_mul_f32_e32 v106, v106, v48
	v_mul_f32_e32 v107, v107, v48
	v_mov_b32_e32 v58, 0
	v_mov_b32_e32 v59, 0
	v_mov_b32_e32 v60, 0
	v_mov_b32_e32 v61, 0
	v_mov_b32_e32 v62, 0
	v_mov_b32_e32 v63, 0
	v_mov_b32_e32 v64, 0
	v_mov_b32_e32 v65, 0
	v_cvt_pk_fp8_f32 v58, v76, v77
	v_cvt_pk_fp8_f32 v59, v80, v81
	v_cvt_pk_fp8_f32 v60, v84, v85
	v_cvt_pk_fp8_f32 v61, v88, v89
	v_cvt_pk_fp8_f32 v62, v92, v93
	v_cvt_pk_fp8_f32 v63, v96, v97
	v_cvt_pk_fp8_f32 v64, v100, v101
	v_cvt_pk_fp8_f32 v65, v104, v105
	v_cvt_pk_fp8_f32 v58, v78, v79 op_sel:[0,0,1]
	v_cvt_pk_fp8_f32 v59, v82, v83 op_sel:[0,0,1]
	v_cvt_pk_fp8_f32 v60, v86, v87 op_sel:[0,0,1]
	v_cvt_pk_fp8_f32 v61, v90, v91 op_sel:[0,0,1]
	v_cvt_pk_fp8_f32 v62, v94, v95 op_sel:[0,0,1]
	v_cvt_pk_fp8_f32 v63, v98, v99 op_sel:[0,0,1]
	v_cvt_pk_fp8_f32 v64, v102, v103 op_sel:[0,0,1]
	v_cvt_pk_fp8_f32 v65, v106, v107 op_sel:[0,0,1]
	s_and_b32 s11, s4, 0x3fff
	s_lshl_b32 s11, s11, 7
	s_lshr_b32 s101, s4, 14
	s_lshl_b32 s101, s101, 25
	s_add_u32 s11, s11, s101
	v_add_u32_e32 v66, s11, v56
	v_add_u32_e32 v67, 0x400000, v66
	v_add_u32_e32 v68, 0x800000, v66
	v_add_u32_e32 v69, 0xc00000, v66
	v_add_u32_e32 v70, 0x1000000, v66
	v_add_u32_e32 v71, 0x1400000, v66
	v_add_u32_e32 v72, 0x1800000, v66
	v_add_u32_e32 v73, 0x1c00000, v66
	global_store_dword v66, v58, s[6:7] nt
	global_store_dword v67, v59, s[6:7] nt
	global_store_dword v68, v60, s[6:7] nt
	global_store_dword v69, v61, s[6:7] nt
	global_store_dword v70, v62, s[6:7] nt
	global_store_dword v71, v63, s[6:7] nt
	global_store_dword v72, v64, s[6:7] nt
	global_store_dword v73, v65, s[6:7] nt
	s_add_u32 s4, s4, s10
	s_cmp_ge_u32 s4, 0x6c00
	s_cbranch_scc1 .Ldfa_done
	s_branch .Ldfa_loop

.Ldfb1_loop:
	s_add_u32 s11, s4, s10
	s_min_u32 s11, s11, 0x7fff
	s_mov_b32 s101, s11
	s_lshl_b32 s11, s101, 13
	v_add_u32_e32 v40, s11, v7
	v_add_u32_e32 v41, 0x1000, v40
	global_load_dwordx4 v[76:79], v40, s[8:9] nt
	global_load_dwordx4 v[80:83], v40, s[8:9] offset:1024 nt
	global_load_dwordx4 v[84:87], v40, s[8:9] offset:2048 nt
	global_load_dwordx4 v[88:91], v40, s[8:9] offset:3072 nt
	global_load_dwordx4 v[92:95], v41, s[8:9] nt
	global_load_dwordx4 v[96:99], v41, s[8:9] offset:1024 nt
	global_load_dwordx4 v[100:103], v41, s[8:9] offset:2048 nt
	global_load_dwordx4 v[104:107], v41, s[8:9] offset:3072 nt
	s_waitcnt vmcnt(8)
	v_max3_f32 v42, |v8|, |v9|, |v10|
	v_max3_f32 v43, |v12|, |v13|, |v14|
	v_max3_f32 v44, |v16|, |v17|, |v18|
	v_max3_f32 v45, |v20|, |v21|, |v22|
	v_max3_f32 v46, |v24|, |v25|, |v26|
	v_max3_f32 v47, |v28|, |v29|, |v30|
	v_max3_f32 v48, |v32|, |v33|, |v34|
	v_max3_f32 v49, |v36|, |v37|, |v38|
	v_max_f32_e64 v42, v42, |v11|
	v_max_f32_e64 v43, v43, |v15|
	v_max_f32_e64 v44, v44, |v19|
	v_max_f32_e64 v45, v45, |v23|
	v_max_f32_e64 v46, v46, |v27|
	v_max_f32_e64 v47, v47, |v31|
	v_max_f32_e64 v48, v48, |v35|
	v_max_f32_e64 v49, v49, |v39|
	v_max3_f32 v42, v42, v43, v44
	v_max3_f32 v45, v45, v46, v47
	v_max3_f32 v42, v42, v45, v48
	v_max_f32_e32 v42, v42, v49
	s_nop 1
	v_max_f32_dpp v43, v42, v42 quad_perm:[1,0,3,2] row_mask:0xf bank_mask:0xf bound_ctrl:1
	s_nop 1
	v_max_f32_dpp v42, v43, v43 quad_perm:[2,3,0,1] row_mask:0xf bank_mask:0xf bound_ctrl:1
	s_nop 1
	v_max_f32_dpp v43, v42, v42 row_half_mirror row_mask:0xf bank_mask:0xf bound_ctrl:1
	s_nop 1
	v_max_f32_dpp v42, v43, v43 row_mirror row_mask:0xf bank_mask:0xf bound_ctrl:1
	s_nop 1
	v_mov_b32_e32 v43, v42
	s_nop 1
	v_permlane16_swap_b32_e32 v42, v43
	v_max_f32_e32 v42, v42, v43
	v_mov_b32_e32 v43, v42
	s_nop 1
	v_permlane32_swap_b32_e32 v42, v43
	v_max_f32_e32 v49, v42, v43
	v_mul_f32_e32 v44, 0x3b124925, v49
	s_lshl_b32 s11, s4, 2
	s_add_u32 s11, s11, 0x12a00000
	v_mov_b32_e32 v45, s11
	s_mov_b64 exec, 1
	global_store_dword v45, v44, s[6:7]
	s_mov_b64 exec, -1
	v_mov_b32_e32 v46, 0x43e00000
	v_div_scale_f32 v42, s[100:101], v49, v49, v46
	v_rcp_f32_e32 v43, v42
	s_nop 0
	v_fma_f32 v44, -v42, v43, 1.0
	v_fmac_f32_e32 v43, v44, v43
	v_div_scale_f32 v44, vcc, v46, v49, v46
	v_mul_f32_e32 v45, v44, v43
	v_fma_f32 v47, -v42, v45, v44
	v_fmac_f32_e32 v45, v47, v43
	v_fma_f32 v42, -v42, v45, v44
	s_nop 1
	v_div_fmas_f32 v42, v42, v43, v45
	v_div_fixup_f32 v42, v42, v49, v46
	v_cmp_lt_f32_e32 vcc, 0, v49
	s_nop 1
	v_cndmask_b32_e32 v48, 0, v42, vcc
	v_mul_f32_e32 v8, v8, v48
	v_mul_f32_e32 v9, v9, v48
	v_mul_f32_e32 v10, v10, v48
	v_mul_f32_e32 v11, v11, v48
	v_mul_f32_e32 v12, v12, v48
	v_mul_f32_e32 v13, v13, v48
	v_mul_f32_e32 v14, v14, v48
	v_mul_f32_e32 v15, v15, v48
	v_mul_f32_e32 v16, v16, v48
	v_mul_f32_e32 v17, v17, v48
	v_mul_f32_e32 v18, v18, v48
	v_mul_f32_e32 v19, v19, v48
	v_mul_f32_e32 v20, v20, v48
	v_mul_f32_e32 v21, v21, v48
	v_mul_f32_e32 v22, v22, v48
	v_mul_f32_e32 v23, v23, v48
	v_mul_f32_e32 v24, v24, v48
	v_mul_f32_e32 v25, v25, v48
	v_mul_f32_e32 v26, v26, v48
	v_mul_f32_e32 v27, v27, v48
	v_mul_f32_e32 v28, v28, v48
	v_mul_f32_e32 v29, v29, v48
	v_mul_f32_e32 v30, v30, v48
	v_mul_f32_e32 v31, v31, v48
	v_mul_f32_e32 v32, v32, v48
	v_mul_f32_e32 v33, v33, v48
	v_mul_f32_e32 v34, v34, v48
	v_mul_f32_e32 v35, v35, v48
	v_mul_f32_e32 v36, v36, v48
	v_mul_f32_e32 v37, v37, v48
	v_mul_f32_e32 v38, v38, v48
	v_mul_f32_e32 v39, v39, v48
	v_mov_b32_e32 v58, 0
	v_mov_b32_e32 v59, 0
	v_mov_b32_e32 v60, 0
	v_mov_b32_e32 v61, 0
	v_mov_b32_e32 v62, 0
	v_mov_b32_e32 v63, 0
	v_mov_b32_e32 v64, 0
	v_mov_b32_e32 v65, 0
	v_cvt_pk_fp8_f32 v58, v8, v9
	v_cvt_pk_fp8_f32 v59, v12, v13
	v_cvt_pk_fp8_f32 v60, v16, v17
	v_cvt_pk_fp8_f32 v61, v20, v21
	v_cvt_pk_fp8_f32 v62, v24, v25
	v_cvt_pk_fp8_f32 v63, v28, v29
	v_cvt_pk_fp8_f32 v64, v32, v33
	v_cvt_pk_fp8_f32 v65, v36, v37
	v_cvt_pk_fp8_f32 v58, v10, v11 op_sel:[0,0,1]
	v_cvt_pk_fp8_f32 v59, v14, v15 op_sel:[0,0,1]
	v_cvt_pk_fp8_f32 v60, v18, v19 op_sel:[0,0,1]
	v_cvt_pk_fp8_f32 v61, v22, v23 op_sel:[0,0,1]
	v_cvt_pk_fp8_f32 v62, v26, v27 op_sel:[0,0,1]
	v_cvt_pk_fp8_f32 v63, v30, v31 op_sel:[0,0,1]
	v_cvt_pk_fp8_f32 v64, v34, v35 op_sel:[0,0,1]
	v_cvt_pk_fp8_f32 v65, v38, v39 op_sel:[0,0,1]
	s_and_b32 s11, s4, 0x3fff
	s_lshl_b32 s11, s11, 7
	s_lshr_b32 s101, s4, 14
	s_lshl_b32 s101, s101, 25
	s_add_u32 s11, s11, s101
	v_add_u32_e32 v66, s11, v56
	v_add_u32_e32 v67, 0x400000, v66
	v_add_u32_e32 v68, 0x800000, v66
	v_add_u32_e32 v69, 0xc00000, v66
	v_add_u32_e32 v70, 0x1000000, v66
	v_add_u32_e32 v71, 0x1400000, v66
	v_add_u32_e32 v72, 0x1800000, v66
	v_add_u32_e32 v73, 0x1c00000, v66
	global_store_dword v66, v58, s[6:7] nt
	global_store_dword v67, v59, s[6:7] nt
	global_store_dword v68, v60, s[6:7] nt
	global_store_dword v69, v61, s[6:7] nt
	global_store_dword v70, v62, s[6:7] nt
	global_store_dword v71, v63, s[6:7] nt
	global_store_dword v72, v64, s[6:7] nt
	global_store_dword v73, v65, s[6:7] nt
	s_add_u32 s4, s4, s10
	s_cmp_ge_u32 s4, 0x8000
	s_cbranch_scc1 .Ldfb1_done
	s_add_u32 s11, s4, s10
	s_min_u32 s11, s11, 0x7fff
	s_mov_b32 s101, s11
	s_lshl_b32 s11, s101, 13
	v_add_u32_e32 v40, s11, v7
	v_add_u32_e32 v41, 0x1000, v40
	global_load_dwordx4 v[8:11], v40, s[8:9] nt
	global_load_dwordx4 v[12:15], v40, s[8:9] offset:1024 nt
	global_load_dwordx4 v[16:19], v40, s[8:9] offset:2048 nt
	global_load_dwordx4 v[20:23], v40, s[8:9] offset:3072 nt
	global_load_dwordx4 v[24:27], v41, s[8:9] nt
	global_load_dwordx4 v[28:31], v41, s[8:9] offset:1024 nt
	global_load_dwordx4 v[32:35], v41, s[8:9] offset:2048 nt
	global_load_dwordx4 v[36:39], v41, s[8:9] offset:3072 nt
	s_waitcnt vmcnt(8)
	v_max3_f32 v42, |v76|, |v77|, |v78|
	v_max3_f32 v43, |v80|, |v81|, |v82|
	v_max3_f32 v44, |v84|, |v85|, |v86|
	v_max3_f32 v45, |v88|, |v89|, |v90|
	v_max3_f32 v46, |v92|, |v93|, |v94|
	v_max3_f32 v47, |v96|, |v97|, |v98|
	v_max3_f32 v48, |v100|, |v101|, |v102|
	v_max3_f32 v49, |v104|, |v105|, |v106|
	v_max_f32_e64 v42, v42, |v79|
	v_max_f32_e64 v43, v43, |v83|
	v_max_f32_e64 v44, v44, |v87|
	v_max_f32_e64 v45, v45, |v91|
	v_max_f32_e64 v46, v46, |v95|
	v_max_f32_e64 v47, v47, |v99|
	v_max_f32_e64 v48, v48, |v103|
	v_max_f32_e64 v49, v49, |v107|
	v_max3_f32 v42, v42, v43, v44
	v_max3_f32 v45, v45, v46, v47
	v_max3_f32 v42, v42, v45, v48
	v_max_f32_e32 v42, v42, v49
	s_nop 1
	v_max_f32_dpp v43, v42, v42 quad_perm:[1,0,3,2] row_mask:0xf bank_mask:0xf bound_ctrl:1
	s_nop 1
	v_max_f32_dpp v42, v43, v43 quad_perm:[2,3,0,1] row_mask:0xf bank_mask:0xf bound_ctrl:1
	s_nop 1
	v_max_f32_dpp v43, v42, v42 row_half_mirror row_mask:0xf bank_mask:0xf bound_ctrl:1
	s_nop 1
	v_max_f32_dpp v42, v43, v43 row_mirror row_mask:0xf bank_mask:0xf bound_ctrl:1
	s_nop 1
	v_mov_b32_e32 v43, v42
	s_nop 1
	v_permlane16_swap_b32_e32 v42, v43
	v_max_f32_e32 v42, v42, v43
	v_mov_b32_e32 v43, v42
	s_nop 1
	v_permlane32_swap_b32_e32 v42, v43
	v_max_f32_e32 v49, v42, v43
	v_mul_f32_e32 v44, 0x3b124925, v49
	s_lshl_b32 s11, s4, 2
	s_add_u32 s11, s11, 0x12a00000
	v_mov_b32_e32 v45, s11
	s_mov_b64 exec, 1
	global_store_dword v45, v44, s[6:7]
	s_mov_b64 exec, -1
	v_mov_b32_e32 v46, 0x43e00000
	v_div_scale_f32 v42, s[100:101], v49, v49, v46
	v_rcp_f32_e32 v43, v42
	s_nop 0
	v_fma_f32 v44, -v42, v43, 1.0
	v_fmac_f32_e32 v43, v44, v43
	v_div_scale_f32 v44, vcc, v46, v49, v46
	v_mul_f32_e32 v45, v44, v43
	v_fma_f32 v47, -v42, v45, v44
	v_fmac_f32_e32 v45, v47, v43
	v_fma_f32 v42, -v42, v45, v44
	s_nop 1
	v_div_fmas_f32 v42, v42, v43, v45
	v_div_fixup_f32 v42, v42, v49, v46
	v_cmp_lt_f32_e32 vcc, 0, v49
	s_nop 1
	v_cndmask_b32_e32 v48, 0, v42, vcc
	v_mul_f32_e32 v76, v76, v48
	v_mul_f32_e32 v77, v77, v48
	v_mul_f32_e32 v78, v78, v48
	v_mul_f32_e32 v79, v79, v48
	v_mul_f32_e32 v80, v80, v48
	v_mul_f32_e32 v81, v81, v48
	v_mul_f32_e32 v82, v82, v48
	v_mul_f32_e32 v83, v83, v48
	v_mul_f32_e32 v84, v84, v48
	v_mul_f32_e32 v85, v85, v48
	v_mul_f32_e32 v86, v86, v48
	v_mul_f32_e32 v87, v87, v48
	v_mul_f32_e32 v88, v88, v48
	v_mul_f32_e32 v89, v89, v48
	v_mul_f32_e32 v90, v90, v48
	v_mul_f32_e32 v91, v91, v48
	v_mul_f32_e32 v92, v92, v48
	v_mul_f32_e32 v93, v93, v48
	v_mul_f32_e32 v94, v94, v48
	v_mul_f32_e32 v95, v95, v48
	v_mul_f32_e32 v96, v96, v48
	v_mul_f32_e32 v97, v97, v48
	v_mul_f32_e32 v98, v98, v48
	v_mul_f32_e32 v99, v99, v48
	v_mul_f32_e32 v100, v100, v48
	v_mul_f32_e32 v101, v101, v48
	v_mul_f32_e32 v102, v102, v48
	v_mul_f32_e32 v103, v103, v48
	v_mul_f32_e32 v104, v104, v48
	v_mul_f32_e32 v105, v105, v48
	v_mul_f32_e32 v106, v106, v48
	v_mul_f32_e32 v107, v107, v48
	v_mov_b32_e32 v58, 0
	v_mov_b32_e32 v59, 0
	v_mov_b32_e32 v60, 0
	v_mov_b32_e32 v61, 0
	v_mov_b32_e32 v62, 0
	v_mov_b32_e32 v63, 0
	v_mov_b32_e32 v64, 0
	v_mov_b32_e32 v65, 0
	v_cvt_pk_fp8_f32 v58, v76, v77
	v_cvt_pk_fp8_f32 v59, v80, v81
	v_cvt_pk_fp8_f32 v60, v84, v85
	v_cvt_pk_fp8_f32 v61, v88, v89
	v_cvt_pk_fp8_f32 v62, v92, v93
	v_cvt_pk_fp8_f32 v63, v96, v97
	v_cvt_pk_fp8_f32 v64, v100, v101
	v_cvt_pk_fp8_f32 v65, v104, v105
	v_cvt_pk_fp8_f32 v58, v78, v79 op_sel:[0,0,1]
	v_cvt_pk_fp8_f32 v59, v82, v83 op_sel:[0,0,1]
	v_cvt_pk_fp8_f32 v60, v86, v87 op_sel:[0,0,1]
	v_cvt_pk_fp8_f32 v61, v90, v91 op_sel:[0,0,1]
	v_cvt_pk_fp8_f32 v62, v94, v95 op_sel:[0,0,1]
	v_cvt_pk_fp8_f32 v63, v98, v99 op_sel:[0,0,1]
	v_cvt_pk_fp8_f32 v64, v102, v103 op_sel:[0,0,1]
	v_cvt_pk_fp8_f32 v65, v106, v107 op_sel:[0,0,1]
	s_and_b32 s11, s4, 0x3fff
	s_lshl_b32 s11, s11, 7
	s_lshr_b32 s101, s4, 14
	s_lshl_b32 s101, s101, 25
	s_add_u32 s11, s11, s101
	v_add_u32_e32 v66, s11, v56
	v_add_u32_e32 v67, 0x400000, v66
	v_add_u32_e32 v68, 0x800000, v66
	v_add_u32_e32 v69, 0xc00000, v66
	v_add_u32_e32 v70, 0x1000000, v66
	v_add_u32_e32 v71, 0x1400000, v66
	v_add_u32_e32 v72, 0x1800000, v66
	v_add_u32_e32 v73, 0x1c00000, v66
	global_store_dword v66, v58, s[6:7] nt
	global_store_dword v67, v59, s[6:7] nt
	global_store_dword v68, v60, s[6:7] nt
	global_store_dword v69, v61, s[6:7] nt
	global_store_dword v70, v62, s[6:7] nt
	global_store_dword v71, v63, s[6:7] nt
	global_store_dword v72, v64, s[6:7] nt
	global_store_dword v73, v65, s[6:7] nt
	s_add_u32 s4, s4, s10
	s_cmp_ge_u32 s4, 0x8000
	s_cbranch_scc1 .Ldfb1_done
	s_branch .Ldfb1_loop

.Ldfb2_loop:
	s_add_u32 s11, s4, s10
	s_min_u32 s11, s11, 0x39ff
	s_mov_b32 s101, s11
	s_lshl_b32 s11, s101, 13
	v_add_u32_e32 v40, s11, v7
	v_add_u32_e32 v41, 0x1000, v40
	global_load_dwordx4 v[76:79], v40, s[8:9] nt
	global_load_dwordx4 v[80:83], v40, s[8:9] offset:1024 nt
	global_load_dwordx4 v[84:87], v40, s[8:9] offset:2048 nt
	global_load_dwordx4 v[88:91], v40, s[8:9] offset:3072 nt
	global_load_dwordx4 v[92:95], v41, s[8:9] nt
	global_load_dwordx4 v[96:99], v41, s[8:9] offset:1024 nt
	global_load_dwordx4 v[100:103], v41, s[8:9] offset:2048 nt
	global_load_dwordx4 v[104:107], v41, s[8:9] offset:3072 nt
	s_waitcnt vmcnt(8)
	v_max3_f32 v42, |v8|, |v9|, |v10|
	v_max3_f32 v43, |v12|, |v13|, |v14|
	v_max3_f32 v44, |v16|, |v17|, |v18|
	v_max3_f32 v45, |v20|, |v21|, |v22|
	v_max3_f32 v46, |v24|, |v25|, |v26|
	v_max3_f32 v47, |v28|, |v29|, |v30|
	v_max3_f32 v48, |v32|, |v33|, |v34|
	v_max3_f32 v49, |v36|, |v37|, |v38|
	v_max_f32_e64 v42, v42, |v11|
	v_max_f32_e64 v43, v43, |v15|
	v_max_f32_e64 v44, v44, |v19|
	v_max_f32_e64 v45, v45, |v23|
	v_max_f32_e64 v46, v46, |v27|
	v_max_f32_e64 v47, v47, |v31|
	v_max_f32_e64 v48, v48, |v35|
	v_max_f32_e64 v49, v49, |v39|
	v_max3_f32 v42, v42, v43, v44
	v_max3_f32 v45, v45, v46, v47
	v_max3_f32 v42, v42, v45, v48
	v_max_f32_e32 v42, v42, v49
	s_nop 1
	v_max_f32_dpp v43, v42, v42 quad_perm:[1,0,3,2] row_mask:0xf bank_mask:0xf bound_ctrl:1
	s_nop 1
	v_max_f32_dpp v42, v43, v43 quad_perm:[2,3,0,1] row_mask:0xf bank_mask:0xf bound_ctrl:1
	s_nop 1
	v_max_f32_dpp v43, v42, v42 row_half_mirror row_mask:0xf bank_mask:0xf bound_ctrl:1
	s_nop 1
	v_max_f32_dpp v42, v43, v43 row_mirror row_mask:0xf bank_mask:0xf bound_ctrl:1
	s_nop 1
	v_mov_b32_e32 v43, v42
	s_nop 1
	v_permlane16_swap_b32_e32 v42, v43
	v_max_f32_e32 v42, v42, v43
	v_mov_b32_e32 v43, v42
	s_nop 1
	v_permlane32_swap_b32_e32 v42, v43
	v_max_f32_e32 v49, v42, v43
	v_mul_f32_e32 v44, 0x3b124925, v49
	s_lshl_b32 s11, s4, 2
	s_add_u32 s11, s11, 0x12a20000
	v_mov_b32_e32 v45, s11
	s_mov_b64 exec, 1
	global_store_dword v45, v44, s[6:7]
	s_mov_b64 exec, -1
	v_mov_b32_e32 v46, 0x43e00000
	v_div_scale_f32 v42, s[100:101], v49, v49, v46
	v_rcp_f32_e32 v43, v42
	s_nop 0
	v_fma_f32 v44, -v42, v43, 1.0
	v_fmac_f32_e32 v43, v44, v43
	v_div_scale_f32 v44, vcc, v46, v49, v46
	v_mul_f32_e32 v45, v44, v43
	v_fma_f32 v47, -v42, v45, v44
	v_fmac_f32_e32 v45, v47, v43
	v_fma_f32 v42, -v42, v45, v44
	s_nop 1
	v_div_fmas_f32 v42, v42, v43, v45
	v_div_fixup_f32 v42, v42, v49, v46
	v_cmp_lt_f32_e32 vcc, 0, v49
	s_nop 1
	v_cndmask_b32_e32 v48, 0, v42, vcc
	v_mul_f32_e32 v8, v8, v48
	v_mul_f32_e32 v9, v9, v48
	v_mul_f32_e32 v10, v10, v48
	v_mul_f32_e32 v11, v11, v48
	v_mul_f32_e32 v12, v12, v48
	v_mul_f32_e32 v13, v13, v48
	v_mul_f32_e32 v14, v14, v48
	v_mul_f32_e32 v15, v15, v48
	v_mul_f32_e32 v16, v16, v48
	v_mul_f32_e32 v17, v17, v48
	v_mul_f32_e32 v18, v18, v48
	v_mul_f32_e32 v19, v19, v48
	v_mul_f32_e32 v20, v20, v48
	v_mul_f32_e32 v21, v21, v48
	v_mul_f32_e32 v22, v22, v48
	v_mul_f32_e32 v23, v23, v48
	v_mul_f32_e32 v24, v24, v48
	v_mul_f32_e32 v25, v25, v48
	v_mul_f32_e32 v26, v26, v48
	v_mul_f32_e32 v27, v27, v48
	v_mul_f32_e32 v28, v28, v48
	v_mul_f32_e32 v29, v29, v48
	v_mul_f32_e32 v30, v30, v48
	v_mul_f32_e32 v31, v31, v48
	v_mul_f32_e32 v32, v32, v48
	v_mul_f32_e32 v33, v33, v48
	v_mul_f32_e32 v34, v34, v48
	v_mul_f32_e32 v35, v35, v48
	v_mul_f32_e32 v36, v36, v48
	v_mul_f32_e32 v37, v37, v48
	v_mul_f32_e32 v38, v38, v48
	v_mul_f32_e32 v39, v39, v48
	v_mov_b32_e32 v58, 0
	v_mov_b32_e32 v59, 0
	v_mov_b32_e32 v60, 0
	v_mov_b32_e32 v61, 0
	v_mov_b32_e32 v62, 0
	v_mov_b32_e32 v63, 0
	v_mov_b32_e32 v64, 0
	v_mov_b32_e32 v65, 0
	v_cvt_pk_fp8_f32 v58, v8, v9
	v_cvt_pk_fp8_f32 v59, v12, v13
	v_cvt_pk_fp8_f32 v60, v16, v17
	v_cvt_pk_fp8_f32 v61, v20, v21
	v_cvt_pk_fp8_f32 v62, v24, v25
	v_cvt_pk_fp8_f32 v63, v28, v29
	v_cvt_pk_fp8_f32 v64, v32, v33
	v_cvt_pk_fp8_f32 v65, v36, v37
	v_cvt_pk_fp8_f32 v58, v10, v11 op_sel:[0,0,1]
	v_cvt_pk_fp8_f32 v59, v14, v15 op_sel:[0,0,1]
	v_cvt_pk_fp8_f32 v60, v18, v19 op_sel:[0,0,1]
	v_cvt_pk_fp8_f32 v61, v22, v23 op_sel:[0,0,1]
	v_cvt_pk_fp8_f32 v62, v26, v27 op_sel:[0,0,1]
	v_cvt_pk_fp8_f32 v63, v30, v31 op_sel:[0,0,1]
	v_cvt_pk_fp8_f32 v64, v34, v35 op_sel:[0,0,1]
	v_cvt_pk_fp8_f32 v65, v38, v39 op_sel:[0,0,1]
	s_and_b32 s11, s4, 0x3fff
	s_lshl_b32 s11, s11, 7
	s_lshr_b32 s101, s4, 14
	s_lshl_b32 s101, s101, 25
	s_add_u32 s11, s11, s101
	v_add_u32_e32 v66, s11, v56
	v_add_u32_e32 v67, 0x400000, v66
	v_add_u32_e32 v68, 0x800000, v66
	v_add_u32_e32 v69, 0xc00000, v66
	v_add_u32_e32 v70, 0x1000000, v66
	v_add_u32_e32 v71, 0x1400000, v66
	v_add_u32_e32 v72, 0x1800000, v66
	v_add_u32_e32 v73, 0x1c00000, v66
	global_store_dword v66, v58, s[6:7] nt
	global_store_dword v67, v59, s[6:7] nt
	global_store_dword v68, v60, s[6:7] nt
	global_store_dword v69, v61, s[6:7] nt
	global_store_dword v70, v62, s[6:7] nt
	global_store_dword v71, v63, s[6:7] nt
	global_store_dword v72, v64, s[6:7] nt
	global_store_dword v73, v65, s[6:7] nt
	s_add_u32 s4, s4, s10
	s_cmp_ge_u32 s4, 0x3a00
	s_cbranch_scc1 .Ldfb2_done
	s_add_u32 s11, s4, s10
	s_min_u32 s11, s11, 0x39ff
	s_mov_b32 s101, s11
	s_lshl_b32 s11, s101, 13
	v_add_u32_e32 v40, s11, v7
	v_add_u32_e32 v41, 0x1000, v40
	global_load_dwordx4 v[8:11], v40, s[8:9] nt
	global_load_dwordx4 v[12:15], v40, s[8:9] offset:1024 nt
	global_load_dwordx4 v[16:19], v40, s[8:9] offset:2048 nt
	global_load_dwordx4 v[20:23], v40, s[8:9] offset:3072 nt
	global_load_dwordx4 v[24:27], v41, s[8:9] nt
	global_load_dwordx4 v[28:31], v41, s[8:9] offset:1024 nt
	global_load_dwordx4 v[32:35], v41, s[8:9] offset:2048 nt
	global_load_dwordx4 v[36:39], v41, s[8:9] offset:3072 nt
	s_waitcnt vmcnt(8)
	v_max3_f32 v42, |v76|, |v77|, |v78|
	v_max3_f32 v43, |v80|, |v81|, |v82|
	v_max3_f32 v44, |v84|, |v85|, |v86|
	v_max3_f32 v45, |v88|, |v89|, |v90|
	v_max3_f32 v46, |v92|, |v93|, |v94|
	v_max3_f32 v47, |v96|, |v97|, |v98|
	v_max3_f32 v48, |v100|, |v101|, |v102|
	v_max3_f32 v49, |v104|, |v105|, |v106|
	v_max_f32_e64 v42, v42, |v79|
	v_max_f32_e64 v43, v43, |v83|
	v_max_f32_e64 v44, v44, |v87|
	v_max_f32_e64 v45, v45, |v91|
	v_max_f32_e64 v46, v46, |v95|
	v_max_f32_e64 v47, v47, |v99|
	v_max_f32_e64 v48, v48, |v103|
	v_max_f32_e64 v49, v49, |v107|
	v_max3_f32 v42, v42, v43, v44
	v_max3_f32 v45, v45, v46, v47
	v_max3_f32 v42, v42, v45, v48
	v_max_f32_e32 v42, v42, v49
	s_nop 1
	v_max_f32_dpp v43, v42, v42 quad_perm:[1,0,3,2] row_mask:0xf bank_mask:0xf bound_ctrl:1
	s_nop 1
	v_max_f32_dpp v42, v43, v43 quad_perm:[2,3,0,1] row_mask:0xf bank_mask:0xf bound_ctrl:1
	s_nop 1
	v_max_f32_dpp v43, v42, v42 row_half_mirror row_mask:0xf bank_mask:0xf bound_ctrl:1
	s_nop 1
	v_max_f32_dpp v42, v43, v43 row_mirror row_mask:0xf bank_mask:0xf bound_ctrl:1
	s_nop 1
	v_mov_b32_e32 v43, v42
	s_nop 1
	v_permlane16_swap_b32_e32 v42, v43
	v_max_f32_e32 v42, v42, v43
	v_mov_b32_e32 v43, v42
	s_nop 1
	v_permlane32_swap_b32_e32 v42, v43
	v_max_f32_e32 v49, v42, v43
	v_mul_f32_e32 v44, 0x3b124925, v49
	s_lshl_b32 s11, s4, 2
	s_add_u32 s11, s11, 0x12a20000
	v_mov_b32_e32 v45, s11
	s_mov_b64 exec, 1
	global_store_dword v45, v44, s[6:7]
	s_mov_b64 exec, -1
	v_mov_b32_e32 v46, 0x43e00000
	v_div_scale_f32 v42, s[100:101], v49, v49, v46
	v_rcp_f32_e32 v43, v42
	s_nop 0
	v_fma_f32 v44, -v42, v43, 1.0
	v_fmac_f32_e32 v43, v44, v43
	v_div_scale_f32 v44, vcc, v46, v49, v46
	v_mul_f32_e32 v45, v44, v43
	v_fma_f32 v47, -v42, v45, v44
	v_fmac_f32_e32 v45, v47, v43
	v_fma_f32 v42, -v42, v45, v44
	s_nop 1
	v_div_fmas_f32 v42, v42, v43, v45
	v_div_fixup_f32 v42, v42, v49, v46
	v_cmp_lt_f32_e32 vcc, 0, v49
	s_nop 1
	v_cndmask_b32_e32 v48, 0, v42, vcc
	v_mul_f32_e32 v76, v76, v48
	v_mul_f32_e32 v77, v77, v48
	v_mul_f32_e32 v78, v78, v48
	v_mul_f32_e32 v79, v79, v48
	v_mul_f32_e32 v80, v80, v48
	v_mul_f32_e32 v81, v81, v48
	v_mul_f32_e32 v82, v82, v48
	v_mul_f32_e32 v83, v83, v48
	v_mul_f32_e32 v84, v84, v48
	v_mul_f32_e32 v85, v85, v48
	v_mul_f32_e32 v86, v86, v48
	v_mul_f32_e32 v87, v87, v48
	v_mul_f32_e32 v88, v88, v48
	v_mul_f32_e32 v89, v89, v48
	v_mul_f32_e32 v90, v90, v48
	v_mul_f32_e32 v91, v91, v48
	v_mul_f32_e32 v92, v92, v48
	v_mul_f32_e32 v93, v93, v48
	v_mul_f32_e32 v94, v94, v48
	v_mul_f32_e32 v95, v95, v48
	v_mul_f32_e32 v96, v96, v48
	v_mul_f32_e32 v97, v97, v48
	v_mul_f32_e32 v98, v98, v48
	v_mul_f32_e32 v99, v99, v48
	v_mul_f32_e32 v100, v100, v48
	v_mul_f32_e32 v101, v101, v48
	v_mul_f32_e32 v102, v102, v48
	v_mul_f32_e32 v103, v103, v48
	v_mul_f32_e32 v104, v104, v48
	v_mul_f32_e32 v105, v105, v48
	v_mul_f32_e32 v106, v106, v48
	v_mul_f32_e32 v107, v107, v48
	v_mov_b32_e32 v58, 0
	v_mov_b32_e32 v59, 0
	v_mov_b32_e32 v60, 0
	v_mov_b32_e32 v61, 0
	v_mov_b32_e32 v62, 0
	v_mov_b32_e32 v63, 0
	v_mov_b32_e32 v64, 0
	v_mov_b32_e32 v65, 0
	v_cvt_pk_fp8_f32 v58, v76, v77
	v_cvt_pk_fp8_f32 v59, v80, v81
	v_cvt_pk_fp8_f32 v60, v84, v85
	v_cvt_pk_fp8_f32 v61, v88, v89
	v_cvt_pk_fp8_f32 v62, v92, v93
	v_cvt_pk_fp8_f32 v63, v96, v97
	v_cvt_pk_fp8_f32 v64, v100, v101
	v_cvt_pk_fp8_f32 v65, v104, v105
	v_cvt_pk_fp8_f32 v58, v78, v79 op_sel:[0,0,1]
	v_cvt_pk_fp8_f32 v59, v82, v83 op_sel:[0,0,1]
	v_cvt_pk_fp8_f32 v60, v86, v87 op_sel:[0,0,1]
	v_cvt_pk_fp8_f32 v61, v90, v91 op_sel:[0,0,1]
	v_cvt_pk_fp8_f32 v62, v94, v95 op_sel:[0,0,1]
	v_cvt_pk_fp8_f32 v63, v98, v99 op_sel:[0,0,1]
	v_cvt_pk_fp8_f32 v64, v102, v103 op_sel:[0,0,1]
	v_cvt_pk_fp8_f32 v65, v106, v107 op_sel:[0,0,1]
	s_and_b32 s11, s4, 0x3fff
	s_lshl_b32 s11, s11, 7
	s_lshr_b32 s101, s4, 14
	s_lshl_b32 s101, s101, 25
	s_add_u32 s11, s11, s101
	v_add_u32_e32 v66, s11, v56
	v_add_u32_e32 v67, 0x400000, v66
	v_add_u32_e32 v68, 0x800000, v66
	v_add_u32_e32 v69, 0xc00000, v66
	v_add_u32_e32 v70, 0x1000000, v66
	v_add_u32_e32 v71, 0x1400000, v66
	v_add_u32_e32 v72, 0x1800000, v66
	v_add_u32_e32 v73, 0x1c00000, v66
	global_store_dword v66, v58, s[6:7] nt
	global_store_dword v67, v59, s[6:7] nt
	global_store_dword v68, v60, s[6:7] nt
	global_store_dword v69, v61, s[6:7] nt
	global_store_dword v70, v62, s[6:7] nt
	global_store_dword v71, v63, s[6:7] nt
	global_store_dword v72, v64, s[6:7] nt
	global_store_dword v73, v65, s[6:7] nt
	s_add_u32 s4, s4, s10
	s_cmp_ge_u32 s4, 0x3a00
	s_cbranch_scc1 .Ldfb2_done
	s_branch .Ldfb2_loop

.Ldfc_loop:
	s_add_u32 s11, s4, s10
	s_min_u32 s11, s11, 0x7fff
	s_mov_b32 s101, s11
	s_lshl_b32 s11, s101, 13
	v_add_u32_e32 v40, s11, v7
	v_add_u32_e32 v41, 0x1000, v40
	global_load_dwordx4 v[76:79], v40, s[8:9] nt
	global_load_dwordx4 v[80:83], v40, s[8:9] offset:1024 nt
	global_load_dwordx4 v[84:87], v40, s[8:9] offset:2048 nt
	global_load_dwordx4 v[88:91], v40, s[8:9] offset:3072 nt
	global_load_dwordx4 v[92:95], v41, s[8:9] nt
	global_load_dwordx4 v[96:99], v41, s[8:9] offset:1024 nt
	global_load_dwordx4 v[100:103], v41, s[8:9] offset:2048 nt
	global_load_dwordx4 v[104:107], v41, s[8:9] offset:3072 nt
	s_waitcnt vmcnt(8)
	v_max3_f32 v42, |v8|, |v9|, |v10|
	v_max3_f32 v43, |v12|, |v13|, |v14|
	v_max3_f32 v44, |v16|, |v17|, |v18|
	v_max3_f32 v45, |v20|, |v21|, |v22|
	v_max3_f32 v46, |v24|, |v25|, |v26|
	v_max3_f32 v47, |v28|, |v29|, |v30|
	v_max3_f32 v48, |v32|, |v33|, |v34|
	v_max3_f32 v49, |v36|, |v37|, |v38|
	v_max_f32_e64 v42, v42, |v11|
	v_max_f32_e64 v43, v43, |v15|
	v_max_f32_e64 v44, v44, |v19|
	v_max_f32_e64 v45, v45, |v23|
	v_max_f32_e64 v46, v46, |v27|
	v_max_f32_e64 v47, v47, |v31|
	v_max_f32_e64 v48, v48, |v35|
	v_max_f32_e64 v49, v49, |v39|
	v_max3_f32 v42, v42, v43, v44
	v_max3_f32 v45, v45, v46, v47
	v_max3_f32 v42, v42, v45, v48
	v_max_f32_e32 v42, v42, v49
	s_nop 1
	v_max_f32_dpp v43, v42, v42 quad_perm:[1,0,3,2] row_mask:0xf bank_mask:0xf bound_ctrl:1
	s_nop 1
	v_max_f32_dpp v42, v43, v43 quad_perm:[2,3,0,1] row_mask:0xf bank_mask:0xf bound_ctrl:1
	s_nop 1
	v_max_f32_dpp v43, v42, v42 row_half_mirror row_mask:0xf bank_mask:0xf bound_ctrl:1
	s_nop 1
	v_max_f32_dpp v42, v43, v43 row_mirror row_mask:0xf bank_mask:0xf bound_ctrl:1
	s_nop 1
	v_mov_b32_e32 v43, v42
	s_nop 1
	v_permlane16_swap_b32_e32 v42, v43
	v_max_f32_e32 v42, v42, v43
	v_mov_b32_e32 v43, v42
	s_nop 1
	v_permlane32_swap_b32_e32 v42, v43
	v_max_f32_e32 v49, v42, v43
	v_mul_f32_e32 v44, 0x3b124925, v49
	s_lshl_b32 s11, s4, 2
	s_add_u32 s11, s11, 0x12a20000
	v_mov_b32_e32 v45, s11
	s_mov_b64 exec, 1
	global_store_dword v45, v44, s[6:7]
	s_mov_b64 exec, -1
	v_mov_b32_e32 v46, 0x43e00000
	v_div_scale_f32 v42, s[100:101], v49, v49, v46
	v_rcp_f32_e32 v43, v42
	s_nop 0
	v_fma_f32 v44, -v42, v43, 1.0
	v_fmac_f32_e32 v43, v44, v43
	v_div_scale_f32 v44, vcc, v46, v49, v46
	v_mul_f32_e32 v45, v44, v43
	v_fma_f32 v47, -v42, v45, v44
	v_fmac_f32_e32 v45, v47, v43
	v_fma_f32 v42, -v42, v45, v44
	s_nop 1
	v_div_fmas_f32 v42, v42, v43, v45
	v_div_fixup_f32 v42, v42, v49, v46
	v_cmp_lt_f32_e32 vcc, 0, v49
	s_nop 1
	v_cndmask_b32_e32 v48, 0, v42, vcc
	v_mul_f32_e32 v8, v8, v48
	v_mul_f32_e32 v9, v9, v48
	v_mul_f32_e32 v10, v10, v48
	v_mul_f32_e32 v11, v11, v48
	v_mul_f32_e32 v12, v12, v48
	v_mul_f32_e32 v13, v13, v48
	v_mul_f32_e32 v14, v14, v48
	v_mul_f32_e32 v15, v15, v48
	v_mul_f32_e32 v16, v16, v48
	v_mul_f32_e32 v17, v17, v48
	v_mul_f32_e32 v18, v18, v48
	v_mul_f32_e32 v19, v19, v48
	v_mul_f32_e32 v20, v20, v48
	v_mul_f32_e32 v21, v21, v48
	v_mul_f32_e32 v22, v22, v48
	v_mul_f32_e32 v23, v23, v48
	v_mul_f32_e32 v24, v24, v48
	v_mul_f32_e32 v25, v25, v48
	v_mul_f32_e32 v26, v26, v48
	v_mul_f32_e32 v27, v27, v48
	v_mul_f32_e32 v28, v28, v48
	v_mul_f32_e32 v29, v29, v48
	v_mul_f32_e32 v30, v30, v48
	v_mul_f32_e32 v31, v31, v48
	v_mul_f32_e32 v32, v32, v48
	v_mul_f32_e32 v33, v33, v48
	v_mul_f32_e32 v34, v34, v48
	v_mul_f32_e32 v35, v35, v48
	v_mul_f32_e32 v36, v36, v48
	v_mul_f32_e32 v37, v37, v48
	v_mul_f32_e32 v38, v38, v48
	v_mul_f32_e32 v39, v39, v48
	v_mov_b32_e32 v58, 0
	v_mov_b32_e32 v59, 0
	v_mov_b32_e32 v60, 0
	v_mov_b32_e32 v61, 0
	v_mov_b32_e32 v62, 0
	v_mov_b32_e32 v63, 0
	v_mov_b32_e32 v64, 0
	v_mov_b32_e32 v65, 0
	v_cvt_pk_fp8_f32 v58, v8, v9
	v_cvt_pk_fp8_f32 v59, v12, v13
	v_cvt_pk_fp8_f32 v60, v16, v17
	v_cvt_pk_fp8_f32 v61, v20, v21
	v_cvt_pk_fp8_f32 v62, v24, v25
	v_cvt_pk_fp8_f32 v63, v28, v29
	v_cvt_pk_fp8_f32 v64, v32, v33
	v_cvt_pk_fp8_f32 v65, v36, v37
	v_cvt_pk_fp8_f32 v58, v10, v11 op_sel:[0,0,1]
	v_cvt_pk_fp8_f32 v59, v14, v15 op_sel:[0,0,1]
	v_cvt_pk_fp8_f32 v60, v18, v19 op_sel:[0,0,1]
	v_cvt_pk_fp8_f32 v61, v22, v23 op_sel:[0,0,1]
	v_cvt_pk_fp8_f32 v62, v26, v27 op_sel:[0,0,1]
	v_cvt_pk_fp8_f32 v63, v30, v31 op_sel:[0,0,1]
	v_cvt_pk_fp8_f32 v64, v34, v35 op_sel:[0,0,1]
	v_cvt_pk_fp8_f32 v65, v38, v39 op_sel:[0,0,1]
	s_and_b32 s11, s4, 0x3fff
	s_lshl_b32 s11, s11, 7
	s_lshr_b32 s101, s4, 14
	s_lshl_b32 s101, s101, 25
	s_add_u32 s11, s11, s101
	v_add_u32_e32 v66, s11, v56
	v_add_u32_e32 v67, 0x400000, v66
	v_add_u32_e32 v68, 0x800000, v66
	v_add_u32_e32 v69, 0xc00000, v66
	v_add_u32_e32 v70, 0x1000000, v66
	v_add_u32_e32 v71, 0x1400000, v66
	v_add_u32_e32 v72, 0x1800000, v66
	v_add_u32_e32 v73, 0x1c00000, v66
	global_store_dword v66, v58, s[6:7] nt
	global_store_dword v67, v59, s[6:7] nt
	global_store_dword v68, v60, s[6:7] nt
	global_store_dword v69, v61, s[6:7] nt
	global_store_dword v70, v62, s[6:7] nt
	global_store_dword v71, v63, s[6:7] nt
	global_store_dword v72, v64, s[6:7] nt
	global_store_dword v73, v65, s[6:7] nt
	s_add_u32 s4, s4, s10
	s_cmp_ge_u32 s4, 0x8000
	s_cbranch_scc1 .Ldfc_done
	s_add_u32 s11, s4, s10
	s_min_u32 s11, s11, 0x7fff
	s_mov_b32 s101, s11
	s_lshl_b32 s11, s101, 13
	v_add_u32_e32 v40, s11, v7
	v_add_u32_e32 v41, 0x1000, v40
	global_load_dwordx4 v[8:11], v40, s[8:9] nt
	global_load_dwordx4 v[12:15], v40, s[8:9] offset:1024 nt
	global_load_dwordx4 v[16:19], v40, s[8:9] offset:2048 nt
	global_load_dwordx4 v[20:23], v40, s[8:9] offset:3072 nt
	global_load_dwordx4 v[24:27], v41, s[8:9] nt
	global_load_dwordx4 v[28:31], v41, s[8:9] offset:1024 nt
	global_load_dwordx4 v[32:35], v41, s[8:9] offset:2048 nt
	global_load_dwordx4 v[36:39], v41, s[8:9] offset:3072 nt
	s_waitcnt vmcnt(8)
	v_max3_f32 v42, |v76|, |v77|, |v78|
	v_max3_f32 v43, |v80|, |v81|, |v82|
	v_max3_f32 v44, |v84|, |v85|, |v86|
	v_max3_f32 v45, |v88|, |v89|, |v90|
	v_max3_f32 v46, |v92|, |v93|, |v94|
	v_max3_f32 v47, |v96|, |v97|, |v98|
	v_max3_f32 v48, |v100|, |v101|, |v102|
	v_max3_f32 v49, |v104|, |v105|, |v106|
	v_max_f32_e64 v42, v42, |v79|
	v_max_f32_e64 v43, v43, |v83|
	v_max_f32_e64 v44, v44, |v87|
	v_max_f32_e64 v45, v45, |v91|
	v_max_f32_e64 v46, v46, |v95|
	v_max_f32_e64 v47, v47, |v99|
	v_max_f32_e64 v48, v48, |v103|
	v_max_f32_e64 v49, v49, |v107|
	v_max3_f32 v42, v42, v43, v44
	v_max3_f32 v45, v45, v46, v47
	v_max3_f32 v42, v42, v45, v48
	v_max_f32_e32 v42, v42, v49
	s_nop 1
	v_max_f32_dpp v43, v42, v42 quad_perm:[1,0,3,2] row_mask:0xf bank_mask:0xf bound_ctrl:1
	s_nop 1
	v_max_f32_dpp v42, v43, v43 quad_perm:[2,3,0,1] row_mask:0xf bank_mask:0xf bound_ctrl:1
	s_nop 1
	v_max_f32_dpp v43, v42, v42 row_half_mirror row_mask:0xf bank_mask:0xf bound_ctrl:1
	s_nop 1
	v_max_f32_dpp v42, v43, v43 row_mirror row_mask:0xf bank_mask:0xf bound_ctrl:1
	s_nop 1
	v_mov_b32_e32 v43, v42
	s_nop 1
	v_permlane16_swap_b32_e32 v42, v43
	v_max_f32_e32 v42, v42, v43
	v_mov_b32_e32 v43, v42
	s_nop 1
	v_permlane32_swap_b32_e32 v42, v43
	v_max_f32_e32 v49, v42, v43
	v_mul_f32_e32 v44, 0x3b124925, v49
	s_lshl_b32 s11, s4, 2
	s_add_u32 s11, s11, 0x12a20000
	v_mov_b32_e32 v45, s11
	s_mov_b64 exec, 1
	global_store_dword v45, v44, s[6:7]
	s_mov_b64 exec, -1
	v_mov_b32_e32 v46, 0x43e00000
	v_div_scale_f32 v42, s[100:101], v49, v49, v46
	v_rcp_f32_e32 v43, v42
	s_nop 0
	v_fma_f32 v44, -v42, v43, 1.0
	v_fmac_f32_e32 v43, v44, v43
	v_div_scale_f32 v44, vcc, v46, v49, v46
	v_mul_f32_e32 v45, v44, v43
	v_fma_f32 v47, -v42, v45, v44
	v_fmac_f32_e32 v45, v47, v43
	v_fma_f32 v42, -v42, v45, v44
	s_nop 1
	v_div_fmas_f32 v42, v42, v43, v45
	v_div_fixup_f32 v42, v42, v49, v46
	v_cmp_lt_f32_e32 vcc, 0, v49
	s_nop 1
	v_cndmask_b32_e32 v48, 0, v42, vcc
	v_mul_f32_e32 v76, v76, v48
	v_mul_f32_e32 v77, v77, v48
	v_mul_f32_e32 v78, v78, v48
	v_mul_f32_e32 v79, v79, v48
	v_mul_f32_e32 v80, v80, v48
	v_mul_f32_e32 v81, v81, v48
	v_mul_f32_e32 v82, v82, v48
	v_mul_f32_e32 v83, v83, v48
	v_mul_f32_e32 v84, v84, v48
	v_mul_f32_e32 v85, v85, v48
	v_mul_f32_e32 v86, v86, v48
	v_mul_f32_e32 v87, v87, v48
	v_mul_f32_e32 v88, v88, v48
	v_mul_f32_e32 v89, v89, v48
	v_mul_f32_e32 v90, v90, v48
	v_mul_f32_e32 v91, v91, v48
	v_mul_f32_e32 v92, v92, v48
	v_mul_f32_e32 v93, v93, v48
	v_mul_f32_e32 v94, v94, v48
	v_mul_f32_e32 v95, v95, v48
	v_mul_f32_e32 v96, v96, v48
	v_mul_f32_e32 v97, v97, v48
	v_mul_f32_e32 v98, v98, v48
	v_mul_f32_e32 v99, v99, v48
	v_mul_f32_e32 v100, v100, v48
	v_mul_f32_e32 v101, v101, v48
	v_mul_f32_e32 v102, v102, v48
	v_mul_f32_e32 v103, v103, v48
	v_mul_f32_e32 v104, v104, v48
	v_mul_f32_e32 v105, v105, v48
	v_mul_f32_e32 v106, v106, v48
	v_mul_f32_e32 v107, v107, v48
	v_mov_b32_e32 v58, 0
	v_mov_b32_e32 v59, 0
	v_mov_b32_e32 v60, 0
	v_mov_b32_e32 v61, 0
	v_mov_b32_e32 v62, 0
	v_mov_b32_e32 v63, 0
	v_mov_b32_e32 v64, 0
	v_mov_b32_e32 v65, 0
	v_cvt_pk_fp8_f32 v58, v76, v77
	v_cvt_pk_fp8_f32 v59, v80, v81
	v_cvt_pk_fp8_f32 v60, v84, v85
	v_cvt_pk_fp8_f32 v61, v88, v89
	v_cvt_pk_fp8_f32 v62, v92, v93
	v_cvt_pk_fp8_f32 v63, v96, v97
	v_cvt_pk_fp8_f32 v64, v100, v101
	v_cvt_pk_fp8_f32 v65, v104, v105
	v_cvt_pk_fp8_f32 v58, v78, v79 op_sel:[0,0,1]
	v_cvt_pk_fp8_f32 v59, v82, v83 op_sel:[0,0,1]
	v_cvt_pk_fp8_f32 v60, v86, v87 op_sel:[0,0,1]
	v_cvt_pk_fp8_f32 v61, v90, v91 op_sel:[0,0,1]
	v_cvt_pk_fp8_f32 v62, v94, v95 op_sel:[0,0,1]
	v_cvt_pk_fp8_f32 v63, v98, v99 op_sel:[0,0,1]
	v_cvt_pk_fp8_f32 v64, v102, v103 op_sel:[0,0,1]
	v_cvt_pk_fp8_f32 v65, v106, v107 op_sel:[0,0,1]
	s_and_b32 s11, s4, 0x3fff
	s_lshl_b32 s11, s11, 7
	s_lshr_b32 s101, s4, 14
	s_lshl_b32 s101, s101, 25
	s_add_u32 s11, s11, s101
	v_add_u32_e32 v66, s11, v56
	v_add_u32_e32 v67, 0x400000, v66
	v_add_u32_e32 v68, 0x800000, v66
	v_add_u32_e32 v69, 0xc00000, v66
	v_add_u32_e32 v70, 0x1000000, v66
	v_add_u32_e32 v71, 0x1400000, v66
	v_add_u32_e32 v72, 0x1800000, v66
	v_add_u32_e32 v73, 0x1c00000, v66
	global_store_dword v66, v58, s[6:7] nt
	global_store_dword v67, v59, s[6:7] nt
	global_store_dword v68, v60, s[6:7] nt
	global_store_dword v69, v61, s[6:7] nt
	global_store_dword v70, v62, s[6:7] nt
	global_store_dword v71, v63, s[6:7] nt
	global_store_dword v72, v64, s[6:7] nt
	global_store_dword v73, v65, s[6:7] nt
	s_add_u32 s4, s4, s10
	s_cmp_ge_u32 s4, 0x8000
	s_cbranch_scc1 .Ldfc_done
	s_branch .Ldfc_loop
